# neighbourhood-attention inner loop: K-slice ds_reads double-buffered two slices ahead (free v240-247) and V^T reads rolled one d-block ahead, counted lgkmcnt
# speedup vs baseline: 1.0045x; 1.0001x over previous
.LBB0_1577:
	s_mul_hi_i32 s21, s20, 0x3000
	s_mulk_i32 s20, 0x3000
	s_add_u32 s8, s38, s20
	v_sub_f32_e32 v67, v67, v169
	v_sub_f32_e32 v66, v66, v169
	s_addc_u32 s9, s39, s21
	v_exp_f32_e32 v140, v66
	v_exp_f32_e32 v141, v67
	v_lshl_add_u64 v[66:67], v[154:155], 1, s[8:9]
	s_add_i32 s8, s89, s95
	s_mov_b32 s9, m0
	s_mov_b32 m0, s8
	s_nop 0
	global_load_lds_dwordx4 v[66:67], off
	s_mov_b32 m0, s9
	s_add_i32 s8, s89, s96
	v_lshl_add_u64 v[66:67], v[66:67], 0, s[30:31]
	s_mov_b32 s9, m0
	s_mov_b32 m0, s8
	s_nop 0
	global_load_lds_dwordx4 v[66:67], off
	s_mov_b32 m0, s9
	s_add_u32 s8, s93, s20
	s_addc_u32 s9, s94, s21
	s_or_b32 s20, s89, 0x4000
	v_lshl_add_u64 v[66:67], v[152:153], 1, s[8:9]
	s_add_i32 s21, s20, s95
	s_mov_b32 s62, m0
	s_mov_b32 m0, s21
	s_nop 0
	global_load_lds_dwordx4 v[66:67], off
	s_mov_b32 m0, s62
	v_lshl_add_u64 v[66:67], v[156:157], 1, s[8:9]
	s_add_i32 s20, s20, s96
	s_mov_b32 s8, m0
	s_mov_b32 m0, s20
	s_nop 0
	global_load_lds_dwordx4 v[66:67], off
	s_mov_b32 m0, s8
	v_sub_f32_e32 v1, v97, v169
	v_sub_f32_e32 v96, v96, v169
	v_sub_f32_e32 v95, v95, v169
	v_sub_f32_e32 v94, v94, v169
	v_sub_f32_e32 v93, v93, v169
	v_sub_f32_e32 v92, v92, v169
	v_sub_f32_e32 v75, v75, v169
	v_sub_f32_e32 v74, v74, v169
	v_sub_f32_e32 v73, v73, v169
	v_sub_f32_e32 v72, v72, v169
	v_sub_f32_e32 v71, v71, v169
	v_sub_f32_e32 v70, v70, v169
	v_sub_f32_e32 v69, v69, v169
	v_sub_f32_e32 v68, v68, v169
	v_sub_f32_e32 v106, v91, v169
	v_sub_f32_e32 v107, v90, v169
	v_sub_f32_e32 v168, v89, v169
	v_sub_f32_e32 v171, v88, v169
	v_sub_f32_e32 v207, v87, v169
	v_sub_f32_e32 v206, v86, v169
	v_sub_f32_e32 v205, v85, v169
	v_sub_f32_e32 v204, v84, v169
	v_sub_f32_e32 v203, v83, v169
	v_sub_f32_e32 v202, v82, v169
	v_sub_f32_e32 v201, v81, v169
	v_sub_f32_e32 v200, v80, v169
	v_sub_f32_e32 v199, v79, v169
	v_sub_f32_e32 v198, v78, v169
	v_sub_f32_e32 v173, v77, v169
	v_sub_f32_e32 v172, v76, v169
	v_exp_f32_e32 v142, v68
	v_exp_f32_e32 v143, v69
	v_exp_f32_e32 v144, v70
	v_exp_f32_e32 v145, v71
	v_exp_f32_e32 v146, v72
	v_exp_f32_e32 v147, v73
	v_exp_f32_e32 v160, v74
	v_exp_f32_e32 v161, v75
	v_exp_f32_e32 v162, v92
	v_exp_f32_e32 v163, v93
	v_exp_f32_e32 v164, v94
	v_exp_f32_e32 v165, v95
	v_exp_f32_e32 v166, v96
	v_exp_f32_e32 v167, v1
	v_add_u32_e32 v1, s91, v194
	v_add_u32_e32 v70, v1, v192
	ds_read_b128 v[66:69], v70 offset:16384
	ds_read_b128 v[70:73], v70 offset:24576
	v_add_u32_e32 v102, v1, v193
	ds_read_b128 v[98:101], v102 offset:16384
	ds_read_b128 v[102:105], v102 offset:24576
	v_add_u32_e32 v248, v1, v187
	ds_read_b128 v[240:243], v248 offset:16384
	ds_read_b128 v[244:247], v248 offset:24576
	v_exp_f32_e32 v172, v172
	s_waitcnt lgkmcnt(5)
	v_mfma_f32_32x32x16_bf16 v[82:97], v[66:69], v[136:139], 0
	v_exp_f32_e32 v173, v173
	v_exp_f32_e32 v198, v198
	v_exp_f32_e32 v199, v199
	v_exp_f32_e32 v200, v200
	v_exp_f32_e32 v201, v201
	v_exp_f32_e32 v202, v202
	v_exp_f32_e32 v203, v203
	s_waitcnt lgkmcnt(4)
	v_mfma_f32_32x32x16_bf16 v[66:81], v[70:73], v[136:139], 0
	v_exp_f32_e32 v204, v204
	v_exp_f32_e32 v205, v205
	v_exp_f32_e32 v206, v206
	v_exp_f32_e32 v207, v207
	v_exp_f32_e32 v208, v171
	v_exp_f32_e32 v209, v168
	v_exp_f32_e32 v210, v107
	s_waitcnt lgkmcnt(3)
	v_mfma_f32_32x32x16_bf16 v[82:97], v[98:101], v[132:135], v[82:97]
	v_exp_f32_e32 v211, v106
	s_waitcnt lgkmcnt(2)
	v_mfma_f32_32x32x16_bf16 v[66:81], v[102:105], v[132:135], v[66:81]
	v_add_u32_e32 v102, v1, v186
	ds_read_b128 v[98:101], v102 offset:16384
	ds_read_b128 v[102:105], v102 offset:24576
	s_waitcnt lgkmcnt(3)
	v_mfma_f32_32x32x16_bf16 v[82:97], v[240:243], v[128:131], v[82:97]
	s_waitcnt lgkmcnt(2)
	v_mfma_f32_32x32x16_bf16 v[66:81], v[244:247], v[128:131], v[66:81]
	v_add_u32_e32 v248, v1, v189
	ds_read_b128 v[240:243], v248 offset:16384
	ds_read_b128 v[244:247], v248 offset:24576
	s_waitcnt lgkmcnt(3)
	v_mfma_f32_32x32x16_bf16 v[82:97], v[98:101], v[124:127], v[82:97]
	s_waitcnt lgkmcnt(2)
	v_mfma_f32_32x32x16_bf16 v[66:81], v[102:105], v[124:127], v[66:81]
	v_add_u32_e32 v102, v1, v190
	ds_read_b128 v[98:101], v102 offset:16384
	ds_read_b128 v[102:105], v102 offset:24576
	s_waitcnt lgkmcnt(3)
	v_mfma_f32_32x32x16_bf16 v[82:97], v[240:243], v[120:123], v[82:97]
	s_waitcnt lgkmcnt(2)
	v_mfma_f32_32x32x16_bf16 v[66:81], v[244:247], v[120:123], v[66:81]
	v_add_u32_e32 v248, v1, v185
	ds_read_b128 v[240:243], v248 offset:16384
	ds_read_b128 v[244:247], v248 offset:24576
	s_waitcnt lgkmcnt(3)
	v_mfma_f32_32x32x16_bf16 v[82:97], v[98:101], v[116:119], v[82:97]
	s_waitcnt lgkmcnt(2)
	v_mfma_f32_32x32x16_bf16 v[66:81], v[102:105], v[116:119], v[66:81]
	v_add_u32_e32 v1, v1, v188
	ds_read_b128 v[98:101], v1 offset:16384
	ds_read_b128 v[102:105], v1 offset:24576
	s_waitcnt lgkmcnt(3)
	v_mfma_f32_32x32x16_bf16 v[82:97], v[240:243], v[112:115], v[82:97]
	s_waitcnt lgkmcnt(2)
	v_mfma_f32_32x32x16_bf16 v[66:81], v[244:247], v[112:115], v[66:81]
	s_waitcnt lgkmcnt(1)
	v_mfma_f32_32x32x16_bf16 v[82:97], v[98:101], v[108:111], v[82:97]
	v_add_f32_e64 v98, v140, 0
	v_add_f32_e64 v99, v141, 0
	v_add_f32_e64 v98, v172, v98
	v_add_f32_e64 v99, v173, v99
	v_add_f32_e64 v98, v142, v98
	v_add_f32_e64 v99, v143, v99
	v_pk_add_f32 v[98:99], v[198:199], v[98:99]
	s_waitcnt lgkmcnt(0)
	v_mfma_f32_32x32x16_bf16 v[66:81], v[102:105], v[108:111], v[66:81]
	v_add_f32_e64 v98, v144, v98
	v_add_f32_e64 v99, v145, v99
	v_add_f32_e64 v98, v200, v98
	v_add_f32_e64 v99, v201, v99
	v_add_f32_e64 v98, v146, v98
	v_add_f32_e64 v99, v147, v99
	v_pk_add_f32 v[98:99], v[202:203], v[98:99]
	s_nop 0
	v_pk_add_f32 v[98:99], v[160:161], v[98:99]
	s_nop 0
	v_pk_add_f32 v[98:99], v[204:205], v[98:99]
	s_nop 0
	v_pk_add_f32 v[98:99], v[162:163], v[98:99]
	s_nop 0
	v_pk_add_f32 v[98:99], v[206:207], v[98:99]
	s_nop 0
	v_pk_add_f32 v[98:99], v[164:165], v[98:99]
	s_nop 0
	v_pk_add_f32 v[98:99], v[208:209], v[98:99]
	s_nop 0
	v_pk_add_f32 v[98:99], v[166:167], v[98:99]
	s_nop 0
	v_pk_add_f32 v[98:99], v[210:211], v[98:99]
	s_nop 0
	v_pk_add_f32 v[106:107], v[98:99], v[98:99] op_sel:[0,1] op_sel_hi:[1,0]
	v_cvt_pk_bf16_f32 v98, v140, v141
	v_cvt_pk_bf16_f32 v99, v142, v143
	v_cvt_pk_bf16_f32 v100, v144, v145
	v_cvt_pk_bf16_f32 v101, v146, v147
	v_cvt_pk_bf16_f32 v102, v160, v161
	s_nop 0
	v_mov_b32_e32 v107, v106
	v_cvt_pk_bf16_f32 v103, v162, v163
	v_cvt_pk_bf16_f32 v104, v164, v165
	v_cvt_pk_bf16_f32 v105, v166, v167
	s_nop 1
	v_permlane32_swap_b32_e32 v106, v107
	v_permlane32_swap_b32_e32 v98, v100
	v_permlane32_swap_b32_e32 v99, v101
	v_permlane32_swap_b32_e32 v102, v104
	v_permlane32_swap_b32_e32 v103, v105
	v_cvt_pk_bf16_f32 v140, v172, v173
	v_cvt_pk_bf16_f32 v141, v198, v199
	v_cvt_pk_bf16_f32 v142, v200, v201
	v_cvt_pk_bf16_f32 v143, v202, v203
	v_cvt_pk_bf16_f32 v144, v204, v205
	v_cvt_pk_bf16_f32 v145, v206, v207
	v_cvt_pk_bf16_f32 v146, v208, v209
	v_cvt_pk_bf16_f32 v147, v210, v211
	s_nop 0
	v_permlane32_swap_b32_e32 v140, v142
	v_permlane32_swap_b32_e32 v141, v143
	v_permlane32_swap_b32_e32 v144, v146
	v_permlane32_swap_b32_e32 v145, v147
	v_or_b32_e32 v1, s19, v148
	ds_read_b64_tr_b16 v[160:161], v1
	ds_read_b64_tr_b16 v[162:163], v1 offset:2048
	ds_read_b64_tr_b16 v[164:165], v1 offset:4096
	ds_read_b64_tr_b16 v[166:167], v1 offset:6144
	ds_read_b64_tr_b16 v[198:199], v1 offset:8192
	ds_read_b64_tr_b16 v[200:201], v1 offset:10240
	ds_read_b64_tr_b16 v[202:203], v1 offset:12288
	ds_read_b64_tr_b16 v[204:205], v1 offset:14336
	s_waitcnt lgkmcnt(6)
	v_mfma_f32_32x32x16_bf16 v[50:65], v[98:101], v[160:163], v[50:65]
	ds_read_b64_tr_b16 v[160:161], v1 offset:512
	ds_read_b64_tr_b16 v[162:163], v1 offset:2560
	s_add_i32 s8, s18, -3
	s_cmp_le_i32 s16, s44
	s_cselect_b32 s18, s8, 0xfffffc18
	s_and_b64 s[8:9], s[40:41], exec
	s_cselect_b32 s20, -1, s18
	s_cmp_lg_u32 s20, -1
	s_cselect_b64 vcc, -1, 0
	s_waitcnt lgkmcnt(6)
	v_mfma_f32_32x32x16_bf16 v[50:65], v[102:105], v[164:167], v[50:65]
	ds_read_b64_tr_b16 v[164:165], v1 offset:4608
	ds_read_b64_tr_b16 v[166:167], v1 offset:6656
	s_cmp_ge_i32 s20, s87
	s_cselect_b64 s[8:9], -1, 0
	s_cmp_lt_i32 s20, s88
	s_cselect_b64 s[18:19], -1, 0
	s_and_b64 s[8:9], s[8:9], s[18:19]
	s_sub_i32 s18, s20, s0
	s_mulk_i32 s18, 0x7c
	s_waitcnt lgkmcnt(6)
	v_mfma_f32_32x32x16_bf16 v[50:65], v[140:143], v[198:201], v[50:65]
	ds_read_b64_tr_b16 v[198:199], v1 offset:8704
	ds_read_b64_tr_b16 v[200:201], v1 offset:10752
	s_waitcnt lgkmcnt(6)
	v_mfma_f32_32x32x16_bf16 v[50:65], v[144:147], v[202:205], v[50:65]
	ds_read_b64_tr_b16 v[202:203], v1 offset:12800
	ds_read_b64_tr_b16 v[204:205], v1 offset:14848
	s_waitcnt lgkmcnt(6)
	v_mfma_f32_32x32x16_bf16 v[34:49], v[98:101], v[160:163], v[34:49]
	ds_read_b64_tr_b16 v[160:161], v1 offset:1024
	ds_read_b64_tr_b16 v[162:163], v1 offset:3072
	s_waitcnt lgkmcnt(6)
	v_mfma_f32_32x32x16_bf16 v[34:49], v[102:105], v[164:167], v[34:49]
	ds_read_b64_tr_b16 v[164:165], v1 offset:5120
	ds_read_b64_tr_b16 v[166:167], v1 offset:7168
	s_waitcnt lgkmcnt(6)
	v_mfma_f32_32x32x16_bf16 v[34:49], v[140:143], v[198:201], v[34:49]
	ds_read_b64_tr_b16 v[198:199], v1 offset:9216
	ds_read_b64_tr_b16 v[200:201], v1 offset:11264
	s_waitcnt lgkmcnt(6)
	v_mfma_f32_32x32x16_bf16 v[34:49], v[144:147], v[202:205], v[34:49]
	ds_read_b64_tr_b16 v[202:203], v1 offset:13312
	ds_read_b64_tr_b16 v[204:205], v1 offset:15360
	s_waitcnt lgkmcnt(6)
	v_mfma_f32_32x32x16_bf16 v[18:33], v[98:101], v[160:163], v[18:33]
	ds_read_b64_tr_b16 v[160:161], v1 offset:1536
	ds_read_b64_tr_b16 v[162:163], v1 offset:3584
	s_waitcnt lgkmcnt(6)
	v_mfma_f32_32x32x16_bf16 v[18:33], v[102:105], v[164:167], v[18:33]
	ds_read_b64_tr_b16 v[164:165], v1 offset:5632
	ds_read_b64_tr_b16 v[166:167], v1 offset:7680
	s_waitcnt lgkmcnt(6)
	v_mfma_f32_32x32x16_bf16 v[18:33], v[140:143], v[198:201], v[18:33]
	ds_read_b64_tr_b16 v[198:199], v1 offset:9728
	ds_read_b64_tr_b16 v[200:201], v1 offset:11776
	s_waitcnt lgkmcnt(6)
	v_mfma_f32_32x32x16_bf16 v[18:33], v[144:147], v[202:205], v[18:33]
	ds_read_b64_tr_b16 v[202:203], v1 offset:13824
	ds_read_b64_tr_b16 v[204:205], v1 offset:15872
	v_cndmask_b32_e64 v1, 0, v150, s[8:9]
	v_cndmask_b32_e32 v1, -1, v1, vcc
	s_waitcnt lgkmcnt(6)
	v_mfma_f32_32x32x16_bf16 v[2:17], v[98:101], v[160:163], v[2:17]
	v_add_u32_e32 v98, s18, v196
	v_add_u32_e32 v98, 0x3a0, v98
	v_mov_b32_e32 v99, s47
	s_waitcnt lgkmcnt(4)
	v_mfma_f32_32x32x16_bf16 v[2:17], v[102:105], v[164:167], v[2:17]
	s_waitcnt lgkmcnt(2)
	v_mfma_f32_32x32x16_bf16 v[2:17], v[140:143], v[198:201], v[2:17]
	v_cndmask_b32_e64 v140, 0, v184, s[8:9]
	s_and_b64 s[8:9], vcc, s[8:9]
	v_cndmask_b32_e64 v142, v99, v98, s[8:9]
	ds_read2_b32 v[98:99], v142 offset1:1
	ds_read2_b32 v[100:101], v142 offset0:2 offset1:3
	ds_read2_b32 v[102:103], v142 offset0:8 offset1:9
	ds_read2_b32 v[104:105], v142 offset0:10 offset1:11
	v_bfe_i32 v141, v1, 0, 1
	s_waitcnt lgkmcnt(3)
	v_bfi_b32 v98, v141, v98, v175
	v_bfe_i32 v141, v1, 1, 1
	v_mfma_f32_32x32x16_bf16 v[2:17], v[144:147], v[202:205], v[2:17]
	v_bfi_b32 v99, v141, v99, v175
	v_fma_f32 v82, v82, s28, v98
	v_fma_f32 v83, v83, s28, v99
	v_bfe_i32 v98, v1, 2, 1
	v_bfe_i32 v99, v1, 3, 1
	s_waitcnt lgkmcnt(2)
	v_bfi_b32 v98, v98, v100, v175
	v_bfi_b32 v99, v99, v101, v175
	s_nop 0
	v_pk_fma_f32 v[84:85], v[84:85], s[28:29], v[98:99] op_sel_hi:[1,0,1]
	v_bfe_i32 v98, v1, 8, 1
	v_bfe_i32 v99, v1, 9, 1
	s_waitcnt lgkmcnt(1)
	v_bfi_b32 v98, v98, v102, v175
	v_bfi_b32 v99, v99, v103, v175
	s_nop 0
	v_pk_fma_f32 v[86:87], v[86:87], s[28:29], v[98:99] op_sel_hi:[1,0,1]
	v_bfe_i32 v98, v1, 10, 1
	v_bfe_i32 v99, v1, 11, 1
	s_waitcnt lgkmcnt(0)
	v_bfi_b32 v98, v98, v104, v175
	v_bfi_b32 v99, v99, v105, v175
	s_nop 0
	v_pk_fma_f32 v[88:89], v[88:89], s[28:29], v[98:99] op_sel_hi:[1,0,1]
	ds_read2_b32 v[98:99], v142 offset0:16 offset1:17
	v_bfe_i32 v141, v1, 16, 1
	ds_read2_b32 v[100:101], v142 offset0:18 offset1:19
	ds_read2_b32 v[102:103], v142 offset0:24 offset1:25
	ds_read2_b32 v[104:105], v142 offset0:26 offset1:27
	s_waitcnt lgkmcnt(3)
	v_bfi_b32 v98, v141, v98, v175
	v_bfe_i32 v141, v1, 17, 1
	v_bfi_b32 v99, v141, v99, v175
	s_nop 0
	v_pk_fma_f32 v[98:99], v[90:91], s[28:29], v[98:99] op_sel_hi:[1,0,1]
	v_bfe_i32 v90, v1, 18, 1
	s_waitcnt lgkmcnt(2)
	v_bfi_b32 v90, v90, v100, v175
	v_bfe_i32 v91, v1, 19, 1
	v_bfi_b32 v91, v91, v101, v175
	s_nop 0
	v_pk_fma_f32 v[92:93], v[92:93], s[28:29], v[90:91] op_sel_hi:[1,0,1]
	v_bfe_i32 v90, v1, 24, 1
	s_waitcnt lgkmcnt(1)
	v_bfi_b32 v90, v90, v102, v175
	v_bfe_i32 v91, v1, 25, 1
	v_bfi_b32 v91, v91, v103, v175
	s_nop 0
	v_pk_fma_f32 v[100:101], v[94:95], s[28:29], v[90:91] op_sel_hi:[1,0,1]
	v_bfe_i32 v90, v1, 26, 1
	v_bfe_i32 v1, v1, 27, 1
	s_waitcnt lgkmcnt(0)
	v_bfi_b32 v90, v90, v104, v175
	v_bfi_b32 v91, v1, v105, v175
	v_cndmask_b32_e32 v1, -1, v140, vcc
	v_pk_fma_f32 v[102:103], v[96:97], s[28:29], v[90:91] op_sel_hi:[1,0,1]
	ds_read2_b32 v[90:91], v142 offset0:32 offset1:33
	v_bfe_i32 v140, v1, 0, 1
	ds_read2_b32 v[94:95], v142 offset0:34 offset1:35
	ds_read2_b32 v[96:97], v142 offset0:40 offset1:41
	ds_read2_b32 v[104:105], v142 offset0:42 offset1:43
	s_waitcnt lgkmcnt(3)
	v_bfi_b32 v90, v140, v90, v175
	v_bfe_i32 v140, v1, 1, 1
	v_bfi_b32 v91, v140, v91, v175
	s_nop 0
	v_pk_fma_f32 v[90:91], v[66:67], s[28:29], v[90:91] op_sel_hi:[1,0,1]
	v_bfe_i32 v66, v1, 2, 1
	v_bfe_i32 v67, v1, 3, 1
	s_waitcnt lgkmcnt(2)
	v_bfi_b32 v66, v66, v94, v175
	v_bfi_b32 v67, v67, v95, v175
	s_nop 0
	v_pk_fma_f32 v[94:95], v[68:69], s[28:29], v[66:67] op_sel_hi:[1,0,1]
	v_bfe_i32 v66, v1, 8, 1
	v_bfe_i32 v67, v1, 9, 1
	s_waitcnt lgkmcnt(1)
	v_bfi_b32 v66, v66, v96, v175
	v_bfi_b32 v67, v67, v97, v175
	s_nop 0
	v_pk_fma_f32 v[96:97], v[70:71], s[28:29], v[66:67] op_sel_hi:[1,0,1]
	v_bfe_i32 v66, v1, 10, 1
	v_bfe_i32 v67, v1, 11, 1
	s_waitcnt lgkmcnt(0)
	v_bfi_b32 v66, v66, v104, v175
	v_bfi_b32 v67, v67, v105, v175
	s_nop 0
	v_pk_fma_f32 v[104:105], v[72:73], s[28:29], v[66:67] op_sel_hi:[1,0,1]
	ds_read2_b32 v[66:67], v142 offset0:48 offset1:49
	ds_read2_b32 v[68:69], v142 offset0:50 offset1:51
	ds_read2_b32 v[140:141], v142 offset0:56 offset1:57
	ds_read2_b32 v[142:143], v142 offset0:58 offset1:59
	v_bfe_i32 v70, v1, 16, 1
	s_waitcnt lgkmcnt(3)
	v_bfi_b32 v66, v70, v66, v175
	v_bfe_i32 v70, v1, 17, 1
	v_bfi_b32 v67, v70, v67, v175
	s_nop 0
	v_pk_fma_f32 v[72:73], v[74:75], s[28:29], v[66:67] op_sel_hi:[1,0,1]
	v_bfe_i32 v66, v1, 18, 1
	s_waitcnt lgkmcnt(2)
	v_bfi_b32 v66, v66, v68, v175
	v_bfe_i32 v67, v1, 19, 1
	v_bfi_b32 v67, v67, v69, v175
	s_nop 0
	v_pk_fma_f32 v[70:71], v[76:77], s[28:29], v[66:67] op_sel_hi:[1,0,1]
	v_bfe_i32 v66, v1, 24, 1
	s_waitcnt lgkmcnt(1)
	v_bfi_b32 v66, v66, v140, v175
	v_bfe_i32 v67, v1, 25, 1
	v_bfi_b32 v67, v67, v141, v175
	s_nop 0
	v_pk_fma_f32 v[68:69], v[78:79], s[28:29], v[66:67] op_sel_hi:[1,0,1]
	v_bfe_i32 v66, v1, 26, 1
	s_waitcnt lgkmcnt(0)
	v_bfi_b32 v66, v66, v142, v175
	v_bfe_i32 v1, v1, 27, 1
	v_bfi_b32 v67, v1, v143, v175
	s_nop 0
	v_pk_fma_f32 v[66:67], v[80:81], s[28:29], v[66:67] op_sel_hi:[1,0,1]
	v_max_f32_e32 v1, v82, v83
	v_max3_f32 v1, v1, v84, v85
	v_max3_f32 v1, v1, v86, v87
	v_max3_f32 v1, v1, v88, v89
	v_max3_f32 v1, v1, v98, v99
	v_max3_f32 v1, v1, v92, v93
	v_max3_f32 v1, v1, v100, v101
	v_max3_f32 v1, v1, v102, v103
	v_max3_f32 v1, v1, v90, v91
	v_max3_f32 v1, v1, v94, v95
	v_max3_f32 v1, v1, v96, v97
	v_max3_f32 v1, v1, v104, v105
	v_max3_f32 v1, v1, v72, v73
	v_max3_f32 v1, v1, v70, v71
	v_max3_f32 v1, v1, v68, v69
	v_max3_f32 v1, v1, v66, v67
	v_mov_b32_e32 v74, v1
	s_nop 1
	v_permlane32_swap_b32_e32 v1, v74
	v_max_f32_e32 v74, v74, v74
	v_max_f32_e32 v1, v1, v1
	v_max_f32_e32 v1, v1, v74
	v_sub_f32_e32 v74, v1, v159
	v_cmp_ge_f32_e32 vcc, s84, v74
	s_cmp_eq_u64 vcc, exec
	s_cbranch_scc0 .LBB0_1585
	v_mov_b32_e32 v168, 1.0
	v_cmp_gt_f32_e32 vcc, 1.0, v168
	s_cbranch_vccz .LBB0_1582
